# speedup vs baseline: 1.0110x; 1.0026x over previous
amdhsa.kernels:
  - .agpr_count:     0
    .args:
      - .actual_access:  read_only
        .address_space:  global
        .offset:         0
        .size:           8
        .value_kind:     global_buffer
      - .actual_access:  read_only
        .address_space:  global
        .offset:         8
        .size:           8
        .value_kind:     global_buffer
      - .actual_access:  read_only
        .address_space:  global
        .offset:         16
        .size:           8
        .value_kind:     global_buffer
      - .actual_access:  read_only
        .address_space:  global
        .offset:         24
        .size:           8
        .value_kind:     global_buffer
      - .actual_access:  read_only
        .address_space:  global
        .offset:         32
        .size:           8
        .value_kind:     global_buffer
      - .actual_access:  read_only
        .address_space:  global
        .offset:         40
        .size:           8
        .value_kind:     global_buffer
      - .actual_access:  read_only
        .address_space:  global
        .offset:         48
        .size:           8
        .value_kind:     global_buffer
      - .actual_access:  write_only
        .address_space:  global
        .offset:         56
        .size:           8
        .value_kind:     global_buffer
    .group_segment_fixed_size: 98304
    .kernarg_segment_align: 8
    .kernarg_segment_size: 64
    .language:       OpenCL C
    .language_version:
      - 2
      - 0
    .max_flat_workgroup_size: 512
    .name:           _Z11k_conv_mfmaPKDF16_PKDv8_DF16_PKfS5_S5_S5_S5_PDF16_
    .private_segment_fixed_size: 0
    .sgpr_count:     36
    .sgpr_spill_count: 0
    .symbol:         _Z11k_conv_mfmaPKDF16_PKDv8_DF16_PKfS5_S5_S5_S5_PDF16_.kd
    .uniform_work_group_size: 1
    .uses_dynamic_stack: false
    .vgpr_count:     164
    .vgpr_spill_count: 0
    .wavefront_size: 64
  - .agpr_count:     0
    .args:
      - .actual_access:  read_only
        .address_space:  global
        .offset:         0
        .size:           8
        .value_kind:     global_buffer
      - .actual_access:  read_only
        .address_space:  global
        .offset:         8
        .size:           8
        .value_kind:     global_buffer
      - .actual_access:  read_only
        .address_space:  global
        .offset:         16
        .size:           8
        .value_kind:     global_buffer
      - .actual_access:  write_only
        .address_space:  global
        .offset:         24
        .size:           8
        .value_kind:     global_buffer
    .group_segment_fixed_size: 25600
    .kernarg_segment_align: 8
    .kernarg_segment_size: 32
    .language:       OpenCL C
    .language_version:
      - 2
      - 0
    .max_flat_workgroup_size: 1024
    .name:           _Z12k_recon_mfmaPKDF16_PKDv8_DF16_PKfPf
    .private_segment_fixed_size: 0
    .sgpr_count:     25
    .sgpr_spill_count: 0
    .symbol:         _Z12k_recon_mfmaPKDF16_PKDv8_DF16_PKfPf.kd
    .uniform_work_group_size: 1
    .uses_dynamic_stack: false
    .vgpr_count:     84
    .vgpr_spill_count: 0
    .wavefront_size: 64
  - .agpr_count:     0
    .args:
      - .actual_access:  read_only
        .address_space:  global
        .offset:         0
        .size:           8
        .value_kind:     global_buffer
      - .actual_access:  read_only
        .address_space:  global
        .offset:         8
        .size:           8
        .value_kind:     global_buffer
      - .actual_access:  read_only
        .address_space:  global
        .offset:         16
        .size:           8
        .value_kind:     global_buffer
      - .actual_access:  write_only
        .address_space:  global
        .offset:         24
        .size:           8
        .value_kind:     global_buffer
      - .actual_access:  write_only
        .address_space:  global
        .offset:         32
        .size:           8
        .value_kind:     global_buffer
      - .actual_access:  write_only
        .address_space:  global
        .offset:         40
        .size:           8
        .value_kind:     global_buffer
      - .actual_access:  write_only
        .address_space:  global
        .offset:         48
        .size:           8
        .value_kind:     global_buffer
      - .actual_access:  write_only
        .address_space:  global
        .offset:         56
        .size:           8
        .value_kind:     global_buffer
      - .actual_access:  write_only
        .address_space:  global
        .offset:         64
        .size:           8
        .value_kind:     global_buffer
    .group_segment_fixed_size: 67600
    .kernarg_segment_align: 8
    .kernarg_segment_size: 72
    .language:       OpenCL C
    .language_version:
      - 2
      - 0
    .max_flat_workgroup_size: 512
    .name:           _Z11k_proj_mfmaPKDF16_PKDv8_DF16_PKfPfPS1_S6_PhS6_PDF16_
    .private_segment_fixed_size: 0
    .sgpr_count:     36
    .sgpr_spill_count: 0
    .symbol:         _Z11k_proj_mfmaPKDF16_PKDv8_DF16_PKfPfPS1_S6_PhS6_PDF16_.kd
    .uniform_work_group_size: 1
    .uses_dynamic_stack: false
    .vgpr_count:     155
    .vgpr_spill_count: 0
    .wavefront_size: 64
  - .agpr_count:     0
    .args:
      - .actual_access:  read_only
        .address_space:  global
        .offset:         0
        .size:           8
        .value_kind:     global_buffer
      - .actual_access:  read_only
        .address_space:  global
        .offset:         8
        .size:           8
        .value_kind:     global_buffer
      - .actual_access:  read_only
        .address_space:  global
        .offset:         16
        .size:           8
        .value_kind:     global_buffer
      - .actual_access:  read_only
        .address_space:  global
        .offset:         24
        .size:           8
        .value_kind:     global_buffer
      - .actual_access:  read_only
        .address_space:  global
        .offset:         32
        .size:           8
        .value_kind:     global_buffer
      - .actual_access:  read_only
        .address_space:  global
        .offset:         40
        .size:           8
        .value_kind:     global_buffer
      - .actual_access:  write_only
        .address_space:  global
        .offset:         48
        .size:           8
        .value_kind:     global_buffer
      - .actual_access:  write_only
        .address_space:  global
        .offset:         56
        .size:           8
        .value_kind:     global_buffer
      - .actual_access:  read_only
        .address_space:  global
        .offset:         64
        .size:           8
        .value_kind:     global_buffer
      - .actual_access:  read_only
        .address_space:  global
        .offset:         72
        .size:           8
        .value_kind:     global_buffer
      - .actual_access:  write_only
        .address_space:  global
        .offset:         80
        .size:           8
        .value_kind:     global_buffer
      - .actual_access:  write_only
        .address_space:  global
        .offset:         88
        .size:           8
        .value_kind:     global_buffer
    .group_segment_fixed_size: 65536
    .kernarg_segment_align: 8
    .kernarg_segment_size: 96
    .language:       OpenCL C
    .language_version:
      - 2
      - 0
    .max_flat_workgroup_size: 512
    .name:           _Z6k_attnPKDv8_DF16_PKfPKhS3_S3_S3_PfS6_S3_S3_PS_S7_
    .private_segment_fixed_size: 0
    .sgpr_count:     34
    .sgpr_spill_count: 0
    .symbol:         _Z6k_attnPKDv8_DF16_PKfPKhS3_S3_S3_PfS6_S3_S3_PS_S7_.kd
    .uniform_work_group_size: 1
    .uses_dynamic_stack: false
    .vgpr_count:     128
    .vgpr_spill_count: 0
    .wavefront_size: 64
  - .agpr_count:     8
    .args:
      - .actual_access:  read_only
        .address_space:  global
        .offset:         0
        .size:           8
        .value_kind:     global_buffer
      - .actual_access:  read_only
        .address_space:  global
        .offset:         8
        .size:           8
        .value_kind:     global_buffer
      - .actual_access:  read_only
        .address_space:  global
        .offset:         16
        .size:           8
        .value_kind:     global_buffer
      - .actual_access:  read_only
        .address_space:  global
        .offset:         24
        .size:           8
        .value_kind:     global_buffer
      - .actual_access:  read_only
        .address_space:  global
        .offset:         32
        .size:           8
        .value_kind:     global_buffer
      - .actual_access:  write_only
        .address_space:  global
        .offset:         40
        .size:           8
        .value_kind:     global_buffer
    .group_segment_fixed_size: 10560
    .kernarg_segment_align: 8
    .kernarg_segment_size: 48
    .language:       OpenCL C
    .language_version:
      - 2
      - 0
    .max_flat_workgroup_size: 256
    .name:           _Z8k_resid2PKDF16_PKfS0_S2_S2_PDF16_
    .private_segment_fixed_size: 0
    .sgpr_count:     38
    .sgpr_spill_count: 0
    .symbol:         _Z8k_resid2PKDF16_PKfS0_S2_S2_PDF16_.kd
    .uniform_work_group_size: 1
    .uses_dynamic_stack: false
    .vgpr_count:     120
    .vgpr_spill_count: 0
    .wavefront_size: 64
  - .agpr_count:     0
    .args:
      - .actual_access:  read_only
        .address_space:  global
        .offset:         0
        .size:           8
        .value_kind:     global_buffer
      - .actual_access:  read_only
        .address_space:  global
        .offset:         8
        .size:           8
        .value_kind:     global_buffer
      - .actual_access:  read_only
        .address_space:  global
        .offset:         16
        .size:           8
        .value_kind:     global_buffer
      - .actual_access:  read_only
        .address_space:  global
        .offset:         24
        .size:           8
        .value_kind:     global_buffer
      - .actual_access:  read_only
        .address_space:  global
        .offset:         32
        .size:           8
        .value_kind:     global_buffer
      - .actual_access:  read_only
        .address_space:  global
        .offset:         40
        .size:           8
        .value_kind:     global_buffer
      - .actual_access:  read_only
        .address_space:  global
        .offset:         48
        .size:           8
        .value_kind:     global_buffer
      - .actual_access:  read_only
        .address_space:  global
        .offset:         56
        .size:           8
        .value_kind:     global_buffer
      - .actual_access:  read_only
        .address_space:  global
        .offset:         64
        .size:           8
        .value_kind:     global_buffer
      - .actual_access:  read_only
        .address_space:  global
        .offset:         72
        .size:           8
        .value_kind:     global_buffer
      - .actual_access:  write_only
        .address_space:  global
        .offset:         80
        .size:           8
        .value_kind:     global_buffer
      - .actual_access:  read_only
        .address_space:  global
        .offset:         88
        .size:           8
        .value_kind:     global_buffer
      - .actual_access:  read_only
        .address_space:  global
        .offset:         96
        .size:           8
        .value_kind:     global_buffer
      - .actual_access:  read_only
        .address_space:  global
        .offset:         104
        .size:           8
        .value_kind:     global_buffer
      - .actual_access:  read_only
        .address_space:  global
        .offset:         112
        .size:           8
        .value_kind:     global_buffer
      - .actual_access:  read_only
        .address_space:  global
        .offset:         120
        .size:           8
        .value_kind:     global_buffer
      - .actual_access:  read_only
        .address_space:  global
        .offset:         128
        .size:           8
        .value_kind:     global_buffer
      - .actual_access:  write_only
        .address_space:  global
        .offset:         136
        .size:           8
        .value_kind:     global_buffer
    .group_segment_fixed_size: 21248
    .kernarg_segment_align: 8
    .kernarg_segment_size: 144
    .language:       OpenCL C
    .language_version:
      - 2
      - 0
    .max_flat_workgroup_size: 512
    .name:           _Z8k_embed2PKfS0_S0_S0_S0_S0_S0_S0_S0_S0_PDF16_S0_S0_S0_S0_S0_S0_PDv8_DF16_
    .private_segment_fixed_size: 0
    .sgpr_count:     37
    .sgpr_spill_count: 0
    .symbol:         _Z8k_embed2PKfS0_S0_S0_S0_S0_S0_S0_S0_S0_PDF16_S0_S0_S0_S0_S0_S0_PDv8_DF16_.kd
    .uniform_work_group_size: 1
    .uses_dynamic_stack: false
    .vgpr_count:     99
    .vgpr_spill_count: 0
    .wavefront_size: 64
